# speedup vs baseline: 1.0062x; 1.0005x over previous
.LBB2_1:
	s_mul_i32 s22, s21, 0xe000
	v_add_u32_e32 v196, s22, v214
	v_add_u32_e32 v197, s22, v215
	s_add_u32 s46, s22, s45
	s_add_i32 s21, s21, 1
	s_waitcnt lgkmcnt(0)
	v_mfma_f32_16x16x32_f16 v[130:133], v[22:25], v[42:45], v[130:133]
	ds_read_b128 v[154:157], v196
	ds_read_b128 v[158:161], v196 offset:2048
	v_mfma_f32_16x16x32_f16 v[98:101], v[18:21], v[42:45], v[98:101]
	ds_read_b128 v[162:165], v196 offset:4096
	ds_read_b128 v[166:169], v196 offset:6144
	v_mfma_f32_16x16x32_f16 v[86:89], v[30:33], v[42:45], v[86:89]
	ds_read_b128 v[170:173], v197 offset:32768
	ds_read_b128 v[174:177], v197 offset:34816
	v_mfma_f32_16x16x32_f16 v[74:77], v[26:29], v[42:45], v[74:77]
	ds_read_b128 v[178:181], v197 offset:36864
	ds_read_b128 v[182:185], v197 offset:38912
	v_mfma_f32_16x16x32_f16 v[70:73], v[42:45], v[34:37], v[70:73]
	ds_read_b128 v[186:189], v197 offset:40960
	ds_read_b128 v[190:193], v197 offset:43008
	v_mfma_f32_16x16x32_f16 v[66:69], v[42:45], v[14:17], v[66:69]
	v_mfma_f32_16x16x32_f16 v[62:65], v[22:25], v[38:41], v[62:65]
	v_mfma_f32_16x16x32_f16 v[58:61], v[18:21], v[38:41], v[58:61]
	v_mfma_f32_16x16x32_f16 v[54:57], v[30:33], v[38:41], v[54:57]
	v_mfma_f32_16x16x32_f16 v[50:53], v[26:29], v[38:41], v[50:53]
	v_mfma_f32_16x16x32_f16 v[46:49], v[38:41], v[34:37], v[46:49]
	v_mfma_f32_16x16x32_f16 v[2:5], v[38:41], v[14:17], v[2:5]
	v_mfma_f32_16x16x32_f16 v[78:81], v[22:25], v[10:13], v[78:81]
	v_mfma_f32_16x16x32_f16 v[82:85], v[18:21], v[10:13], v[82:85]
	v_mfma_f32_16x16x32_f16 v[90:93], v[30:33], v[10:13], v[90:93]
	v_mfma_f32_16x16x32_f16 v[94:97], v[26:29], v[10:13], v[94:97]
	v_mfma_f32_16x16x32_f16 v[102:105], v[10:13], v[34:37], v[102:105]
	v_mfma_f32_16x16x32_f16 v[106:109], v[10:13], v[14:17], v[106:109]
	v_mfma_f32_16x16x32_f16 v[110:113], v[22:25], v[6:9], v[110:113]
	v_mfma_f32_16x16x32_f16 v[114:117], v[18:21], v[6:9], v[114:117]
	v_mfma_f32_16x16x32_f16 v[118:121], v[30:33], v[6:9], v[118:121]
	v_mfma_f32_16x16x32_f16 v[122:125], v[26:29], v[6:9], v[122:125]
	v_mfma_f32_16x16x32_f16 v[134:137], v[6:9], v[34:37], v[134:137]
	v_mfma_f32_16x16x32_f16 v[126:129], v[6:9], v[14:17], v[126:129]
	s_cmp_lg_u32 s21, 2
	s_cselect_b32 s21, s21, 0
	s_mul_i32 s22, s21, 0xe000
	v_add_u32_e32 v196, s22, v146
	v_add_u32_e32 v197, s22, v153
	s_waitcnt vmcnt(0) lgkmcnt(0)
	s_barrier
	s_mov_b32 m0, s46
	s_nop 0
	global_load_lds_dwordx4 v194, s[24:25]
	s_add_u32 m0, s46, 0x8000
	s_nop 0
	global_load_lds_dwordx4 v194, s[32:33]
	s_add_u32 m0, s46, 0x2000
	s_nop 0
	global_load_lds_dwordx4 v194, s[26:27]
	s_add_u32 m0, s46, 0xa000
	s_nop 0
	global_load_lds_dwordx4 v194, s[34:35]
	s_add_u32 m0, s46, 0x4000
	s_nop 0
	global_load_lds_dwordx4 v194, s[28:29]
	s_add_u32 m0, s46, 0xc000
	s_nop 0
	global_load_lds_dwordx4 v194, s[36:37]
	s_add_u32 m0, s46, 0x6000
	s_nop 0
	global_load_lds_dwordx4 v194, s[30:31]
	v_add_u32_e32 v194, 0x80, v194
	v_mfma_f32_16x16x32_f16 v[130:133], v[170:173], v[154:157], v[130:133]
	ds_read_b128 v[42:45], v196
	ds_read_b128 v[38:41], v196 offset:2048
	v_mfma_f32_16x16x32_f16 v[98:101], v[174:177], v[154:157], v[98:101]
	ds_read_b128 v[10:13], v196 offset:4096
	ds_read_b128 v[6:9], v196 offset:6144
	v_mfma_f32_16x16x32_f16 v[86:89], v[178:181], v[154:157], v[86:89]
	ds_read_b128 v[22:25], v197 offset:32768
	ds_read_b128 v[18:21], v197 offset:34816
	v_mfma_f32_16x16x32_f16 v[74:77], v[182:185], v[154:157], v[74:77]
	ds_read_b128 v[30:33], v197 offset:36864
	ds_read_b128 v[26:29], v197 offset:38912
	v_mfma_f32_16x16x32_f16 v[70:73], v[154:157], v[186:189], v[70:73]
	ds_read_b128 v[34:37], v197 offset:40960
	ds_read_b128 v[14:17], v197 offset:43008
	v_mfma_f32_16x16x32_f16 v[66:69], v[154:157], v[190:193], v[66:69]
	v_mfma_f32_16x16x32_f16 v[62:65], v[170:173], v[158:161], v[62:65]
	v_mfma_f32_16x16x32_f16 v[58:61], v[174:177], v[158:161], v[58:61]
	v_mfma_f32_16x16x32_f16 v[54:57], v[178:181], v[158:161], v[54:57]
	v_mfma_f32_16x16x32_f16 v[50:53], v[182:185], v[158:161], v[50:53]
	v_mfma_f32_16x16x32_f16 v[46:49], v[158:161], v[186:189], v[46:49]
	v_mfma_f32_16x16x32_f16 v[2:5], v[158:161], v[190:193], v[2:5]
	v_mfma_f32_16x16x32_f16 v[78:81], v[170:173], v[162:165], v[78:81]
	v_mfma_f32_16x16x32_f16 v[82:85], v[174:177], v[162:165], v[82:85]
	v_mfma_f32_16x16x32_f16 v[90:93], v[178:181], v[162:165], v[90:93]
	v_mfma_f32_16x16x32_f16 v[94:97], v[182:185], v[162:165], v[94:97]
	v_mfma_f32_16x16x32_f16 v[102:105], v[162:165], v[186:189], v[102:105]
	v_mfma_f32_16x16x32_f16 v[106:109], v[162:165], v[190:193], v[106:109]
	v_mfma_f32_16x16x32_f16 v[110:113], v[170:173], v[166:169], v[110:113]
	v_mfma_f32_16x16x32_f16 v[114:117], v[174:177], v[166:169], v[114:117]
	v_mfma_f32_16x16x32_f16 v[118:121], v[178:181], v[166:169], v[118:121]
	v_mfma_f32_16x16x32_f16 v[122:125], v[182:185], v[166:169], v[122:125]
	v_mfma_f32_16x16x32_f16 v[134:137], v[166:169], v[186:189], v[134:137]
	v_mfma_f32_16x16x32_f16 v[126:129], v[166:169], v[190:193], v[126:129]
	s_add_u32 s0, s0, 0x80
	s_addc_u32 s1, s1, 0
	s_cmpk_eq_i32 s0, 0x700
	s_cbranch_scc0 .LBB2_1
	s_waitcnt lgkmcnt(0)
	v_mfma_f32_16x16x32_f16 v[130:133], v[22:25], v[42:45], v[130:133]
	ds_read_b128 v[140:143], v214
	ds_read_b128 v[154:157], v214 offset:2048
	v_mfma_f32_16x16x32_f16 v[98:101], v[18:21], v[42:45], v[98:101]
	ds_read_b128 v[158:161], v214 offset:4096
	ds_read_b128 v[162:165], v214 offset:6144
	v_mfma_f32_16x16x32_f16 v[86:89], v[30:33], v[42:45], v[86:89]
	ds_read_b128 v[166:169], v215 offset:32768
	ds_read_b128 v[170:173], v215 offset:34816
	v_mfma_f32_16x16x32_f16 v[74:77], v[26:29], v[42:45], v[74:77]
	ds_read_b128 v[174:177], v215 offset:36864
	ds_read_b128 v[178:181], v215 offset:38912
	v_mfma_f32_16x16x32_f16 v[70:73], v[42:45], v[34:37], v[70:73]
	ds_read_b128 v[182:185], v215 offset:40960
	ds_read_b128 v[186:189], v215 offset:43008
	v_mfma_f32_16x16x32_f16 v[42:45], v[42:45], v[14:17], v[66:69]
	v_mfma_f32_16x16x32_f16 v[62:65], v[22:25], v[38:41], v[62:65]
	v_mfma_f32_16x16x32_f16 v[58:61], v[18:21], v[38:41], v[58:61]
	v_mfma_f32_16x16x32_f16 v[54:57], v[30:33], v[38:41], v[54:57]
	v_mfma_f32_16x16x32_f16 v[50:53], v[26:29], v[38:41], v[50:53]
	v_mfma_f32_16x16x32_f16 v[46:49], v[38:41], v[34:37], v[46:49]
	v_mfma_f32_16x16x32_f16 v[2:5], v[38:41], v[14:17], v[2:5]
	v_mfma_f32_16x16x32_f16 v[38:41], v[22:25], v[10:13], v[78:81]
	v_mfma_f32_16x16x32_f16 v[66:69], v[18:21], v[10:13], v[82:85]
	v_mfma_f32_16x16x32_f16 v[78:81], v[30:33], v[10:13], v[90:93]
	v_mfma_f32_16x16x32_f16 v[82:85], v[26:29], v[10:13], v[94:97]
	v_mfma_f32_16x16x32_f16 v[90:93], v[10:13], v[34:37], v[102:105]
	v_mfma_f32_16x16x32_f16 v[94:97], v[10:13], v[14:17], v[106:109]
	v_mfma_f32_16x16x32_f16 v[22:25], v[22:25], v[6:9], v[110:113]
	v_mfma_f32_16x16x32_f16 v[102:105], v[18:21], v[6:9], v[114:117]
	v_or_b32_e32 v21, v151, v152
	v_and_b32_e32 v20, 63, v0
	v_mfma_f32_16x16x32_f16 v[30:33], v[30:33], v[6:9], v[118:121]
	v_mfma_f32_16x16x32_f16 v[26:29], v[26:29], v[6:9], v[122:125]
	v_mfma_f32_16x16x32_f16 v[34:37], v[6:9], v[34:37], v[134:137]
	v_mfma_f32_16x16x32_f16 v[6:9], v[6:9], v[14:17], v[126:129]
	v_add_u32_e32 v10, 0x16800, v21
	s_waitcnt vmcnt(0) lgkmcnt(0)
	s_waitcnt lgkmcnt(0)
	v_mfma_f32_16x16x32_f16 v[16:19], v[166:169], v[140:143], v[130:133]
	s_barrier
	ds_read_b128 v[106:109], v146 offset:57344
	ds_read_b128 v[110:113], v146 offset:59392
	v_mfma_f32_16x16x32_f16 v[98:101], v[170:173], v[140:143], v[98:101]
	ds_read_b128 v[114:117], v146 offset:61440
	ds_read_b128 v[12:15], v146 offset:63488
	v_add_u32_e32 v0, 0x16000, v21
	v_mfma_f32_16x16x32_f16 v[86:89], v[174:177], v[140:143], v[86:89]
	ds_read_b128 v[122:125], v10
	v_add_u32_e32 v10, 0x17000, v21
	ds_read_b128 v[118:121], v0
	v_mfma_f32_16x16x32_f16 v[74:77], v[178:181], v[140:143], v[74:77]
	ds_read_b128 v[126:129], v10
	v_add_u32_e32 v10, 0x17800, v21
	ds_read_b128 v[130:133], v10
	v_mfma_f32_16x16x32_f16 v[70:73], v[140:143], v[182:185], v[70:73]
	ds_read_b128 v[134:137], v0 offset:8192
	ds_read_b128 v[190:193], v0 offset:10240
	v_mfma_f32_16x16x32_f16 v[42:45], v[140:143], v[186:189], v[42:45]
	v_mfma_f32_16x16x32_f16 v[62:65], v[166:169], v[154:157], v[62:65]
	v_mfma_f32_16x16x32_f16 v[58:61], v[170:173], v[154:157], v[58:61]
	v_mfma_f32_16x16x32_f16 v[54:57], v[174:177], v[154:157], v[54:57]
	v_mfma_f32_16x16x32_f16 v[50:53], v[178:181], v[154:157], v[50:53]
	v_mfma_f32_16x16x32_f16 v[46:49], v[154:157], v[182:185], v[46:49]
	v_mfma_f32_16x16x32_f16 v[140:143], v[154:157], v[186:189], v[2:5]
	v_mfma_f32_16x16x32_f16 v[38:41], v[166:169], v[158:161], v[38:41]
	v_mfma_f32_16x16x32_f16 v[66:69], v[170:173], v[158:161], v[66:69]
	v_mfma_f32_16x16x32_f16 v[78:81], v[174:177], v[158:161], v[78:81]
	v_mfma_f32_16x16x32_f16 v[82:85], v[178:181], v[158:161], v[82:85]
	v_mfma_f32_16x16x32_f16 v[90:93], v[158:161], v[182:185], v[90:93]
	v_mfma_f32_16x16x32_f16 v[94:97], v[158:161], v[186:189], v[94:97]
	v_mfma_f32_16x16x32_f16 v[22:25], v[166:169], v[162:165], v[22:25]
	v_mfma_f32_16x16x32_f16 v[102:105], v[170:173], v[162:165], v[102:105]
	v_mfma_f32_16x16x32_f16 v[30:33], v[174:177], v[162:165], v[30:33]
	v_mfma_f32_16x16x32_f16 v[26:29], v[178:181], v[162:165], v[26:29]
	v_mfma_f32_16x16x32_f16 v[34:37], v[162:165], v[182:185], v[34:37]
	v_mfma_f32_16x16x32_f16 v[152:155], v[162:165], v[186:189], v[6:9]
	s_waitcnt lgkmcnt(0)
	v_mfma_f32_16x16x32_f16 v[156:159], v[118:121], v[106:109], v[16:19]
	s_movk_i32 s0, 0x7c0
	v_add_u32_e32 v216, 0x16000, v215
	ds_read_b128 v[202:205], v216 offset:8192
	ds_read_b128 v[206:209], v216 offset:10240
	v_lshlrev_b32_e32 v16, 6, v144
	v_mov_b32_e32 v17, 0
	v_mov_b32_e32 v139, v17
	v_lshl_add_u64 v[4:5], s[6:7], 0, v[16:17]
	v_lshl_add_u64 v[8:9], v[4:5], 0, v[138:139]
	s_waitcnt vmcnt(0)
	v_lshlrev_b32_e32 v4, 5, v150
	v_lshl_add_u64 v[2:3], s[4:5], 0, v[16:17]
	v_ashrrev_i32_e32 v5, 31, v4
	v_lshl_add_u64 v[2:3], v[2:3], 0, v[138:139]
	v_lshlrev_b64 v[4:5], 2, v[4:5]
	v_lshl_add_u64 v[6:7], v[2:3], 0, v[4:5]
	v_lshl_add_u64 v[4:5], v[8:9], 0, v[4:5]
	v_mfma_f32_16x16x32_f16 v[98:101], v[122:125], v[106:109], v[98:101]
	global_load_dwordx4 v[160:163], v[6:7], off
	v_lshlrev_b32_e32 v18, 5, v147
	v_ashrrev_i32_e32 v19, 31, v18
	v_mfma_f32_16x16x32_f16 v[86:89], v[126:129], v[106:109], v[86:89]
	v_lshlrev_b64 v[18:19], 2, v[18:19]
	ds_read_b128 v[172:175], v214 offset:61440
	ds_read_b128 v[176:179], v214 offset:63488
	v_mfma_f32_16x16x32_f16 v[74:77], v[130:133], v[106:109], v[74:77]
	v_mfma_f32_16x16x32_f16 v[70:73], v[106:109], v[134:137], v[70:73]
	v_mfma_f32_16x16x32_f16 v[42:45], v[106:109], v[190:193], v[42:45]
	global_load_dwordx4 v[106:109], v[4:5], off
	v_lshlrev_b32_e32 v4, 5, v149
	v_ashrrev_i32_e32 v5, 31, v4
	v_lshlrev_b64 v[4:5], 2, v[4:5]
	v_lshl_add_u64 v[6:7], v[2:3], 0, v[4:5]
	v_lshl_add_u64 v[4:5], v[8:9], 0, v[4:5]
	global_load_dwordx4 v[168:171], v[4:5], off
	global_load_dwordx4 v[164:167], v[6:7], off
	v_lshlrev_b32_e32 v4, 5, v148
	v_ashrrev_i32_e32 v5, 31, v4
	v_lshlrev_b64 v[10:11], 2, v[4:5]
	v_lshl_add_u64 v[4:5], v[2:3], 0, v[10:11]
	v_lshl_add_u64 v[10:11], v[8:9], 0, v[10:11]
	global_load_dwordx4 v[210:213], v[10:11], off
	v_lshl_add_u64 v[2:3], v[2:3], 0, v[18:19]
	global_load_dwordx4 v[4:7], v[4:5], off
	v_lshl_add_u64 v[8:9], v[8:9], 0, v[18:19]
	v_add_u32_e32 v18, 0x16000, v215
	v_ashrrev_i32_e32 v10, 7, v145
	ds_read_b128 v[180:183], v18
	v_add_u32_e32 v18, 0x17000, v215
	v_and_b32_e32 v10, -16, v10
	v_add_u32_e32 v19, 0x16800, v215
	ds_read_b128 v[194:197], v18
	v_add_u32_e32 v18, s20, v10
	global_load_dwordx4 v[8:11], v[8:9], off
	ds_read_b128 v[184:187], v19
	v_add_u32_e32 v19, 0x17800, v215
	v_and_or_b32 v21, v145, s0, v1
	global_load_dwordx4 v[0:3], v[2:3], off
	v_mfma_f32_16x16x32_f16 v[62:65], v[118:121], v[110:113], v[62:65]
	ds_read_b128 v[198:201], v19
	v_ashrrev_i32_e32 v19, 31, v18
	ds_read_b128 v[148:151], v214 offset:59392
	v_mfma_f32_16x16x32_f16 v[58:61], v[122:125], v[110:113], v[58:61]
	v_mfma_f32_16x16x32_f16 v[54:57], v[126:129], v[110:113], v[54:57]
	v_mfma_f32_16x16x32_f16 v[50:53], v[130:133], v[110:113], v[50:53]
	v_mfma_f32_16x16x32_f16 v[46:49], v[110:113], v[134:137], v[46:49]
	v_mfma_f32_16x16x32_f16 v[110:113], v[110:113], v[190:193], v[140:143]
	s_nop 2
	ds_read_b128 v[140:143], v214 offset:57344
	v_mfma_f32_16x16x32_f16 v[38:41], v[118:121], v[114:117], v[38:41]
	v_mfma_f32_16x16x32_f16 v[66:69], v[122:125], v[114:117], v[66:69]
	v_mfma_f32_16x16x32_f16 v[78:81], v[126:129], v[114:117], v[78:81]
	v_mfma_f32_16x16x32_f16 v[82:85], v[130:133], v[114:117], v[82:85]
	v_mfma_f32_16x16x32_f16 v[90:93], v[114:117], v[134:137], v[90:93]
	v_mfma_f32_16x16x32_f16 v[94:97], v[114:117], v[190:193], v[94:97]
	s_waitcnt lgkmcnt(0)
	v_mfma_f32_16x16x32_f16 v[114:117], v[180:183], v[140:143], v[156:159]
	v_mfma_f32_16x16x32_f16 v[98:101], v[184:187], v[140:143], v[98:101]
	v_mfma_f32_16x16x32_f16 v[22:25], v[118:121], v[12:15], v[22:25]
	s_waitcnt vmcnt(6)
	s_nop 4
	v_pk_mul_f32 v[120:121], v[114:115], v[106:107] op_sel_hi:[1,0]
	v_lshlrev_b64 v[118:119], 17, v[18:19]
	v_lshl_or_b32 v118, v21, 6, v118
	v_mfma_f32_16x16x32_f16 v[102:105], v[122:125], v[12:15], v[102:105]
	v_mul_f32_e64 v122, v116, v107
	v_mul_f32_e64 v123, v117, v107
	v_pk_fma_f32 v[124:125], v[114:115], v[160:161], v[120:121] op_sel:[0,0,1] op_sel_hi:[1,1,0] neg_lo:[0,0,1] neg_hi:[0,0,1]
	v_pk_fma_f32 v[114:115], v[114:115], v[160:161], v[120:121] op_sel:[0,0,1] op_sel_hi:[1,0,0]
	v_pk_fma_f32 v[120:121], v[116:117], v[160:161], v[122:123] op_sel:[0,1,1] op_sel_hi:[1,1,0] neg_lo:[0,0,1] neg_hi:[0,0,1]
	v_pk_fma_f32 v[116:117], v[116:117], v[160:161], v[122:123] op_sel:[0,1,1] op_sel_hi:[1,1,0]
	v_cvt_pk_f16_f32 v114, v124, v115
	v_cvt_pk_f16_f32 v115, v120, v117
	v_pk_mul_f32 v[116:117], v[98:99], v[108:109] op_sel_hi:[1,0]
	v_mov_b32_e32 v122, v163
	v_pk_fma_f32 v[120:121], v[98:99], v[162:163], v[116:117] op_sel:[0,0,1] op_sel_hi:[1,1,0] neg_lo:[0,0,1] neg_hi:[0,0,1]
	v_pk_fma_f32 v[98:99], v[98:99], v[162:163], v[116:117] op_sel:[0,0,1] op_sel_hi:[1,0,0]
	v_mfma_f32_16x16x32_f16 v[30:33], v[126:129], v[12:15], v[30:33]
	v_cvt_pk_f16_f32 v116, v120, v99
	v_mov_b32_e32 v120, v109
	v_pk_mul_f32 v[98:99], v[100:101], v[120:121] op_sel_hi:[1,0]
	v_mfma_f32_16x16x32_f16 v[26:29], v[130:133], v[12:15], v[26:29]
	v_fma_f32 v124, v100, v122, -v99
	v_fma_f32 v125, v101, v122, -v98
	v_pk_fma_f32 v[98:99], v[100:101], v[122:123], v[98:99] op_sel:[0,0,1] op_sel_hi:[1,0,0]
	s_nop 0
	v_cvt_pk_f16_f32 v117, v124, v99
	v_lshlrev_b64 v[124:125], 1, v[118:119]
	v_lshl_add_u64 v[126:127], s[10:11], 0, v[124:125]
	v_mfma_f32_16x16x32_f16 v[34:37], v[12:15], v[134:137], v[34:37]
	v_mfma_f32_16x16x32_f16 v[98:101], v[12:15], v[190:193], v[152:155]
	v_lshl_add_u64 v[12:13], v[126:127], 0, v[16:17]
	v_lshl_add_u64 v[126:127], v[12:13], 0, v[138:139]
	global_store_dwordx4 v[126:127], v[114:117], off sc1
	v_mfma_f32_16x16x32_f16 v[12:15], v[194:197], v[140:143], v[86:89]
	v_mfma_f32_16x16x32_f16 v[74:77], v[198:201], v[140:143], v[74:77]
	v_mfma_f32_16x16x32_f16 v[58:61], v[184:187], v[148:151], v[58:61]
	s_nop 5
	v_mul_f32_e64 v86, v12, v106
	v_mul_f32_e64 v87, v13, v106
	v_pk_fma_f32 v[88:89], v[12:13], v[160:161], v[86:87] op_sel:[0,0,1] op_sel_hi:[1,1,0] neg_lo:[0,0,1] neg_hi:[0,0,1]
	v_pk_fma_f32 v[12:13], v[12:13], v[160:161], v[86:87] op_sel:[0,0,1] op_sel_hi:[1,0,0]
	v_mfma_f32_16x16x32_f16 v[54:57], v[194:197], v[148:151], v[54:57]
	v_cvt_pk_f16_f32 v86, v88, v13
	v_pk_mul_f32 v[12:13], v[14:15], v[106:107] op_sel:[0,1]
	s_nop 0
	v_pk_fma_f32 v[88:89], v[14:15], v[160:161], v[12:13] op_sel:[0,1,1] op_sel_hi:[1,1,0] neg_lo:[0,0,1] neg_hi:[0,0,1]
	v_pk_fma_f32 v[12:13], v[14:15], v[160:161], v[12:13] op_sel:[0,1,1] op_sel_hi:[1,1,0]
	v_mfma_f32_16x16x32_f16 v[50:53], v[198:201], v[148:151], v[50:53]
	v_cvt_pk_f16_f32 v87, v88, v13
	v_pk_mul_f32 v[88:89], v[74:75], v[108:109] op_sel_hi:[1,0]
	v_mfma_f32_16x16x32_f16 v[12:15], v[140:143], v[206:209], v[42:45]
	s_nop 2
	v_fma_f32 v42, v74, v162, -v89
	v_fma_f32 v43, v75, v163, -v88
	v_pk_fma_f32 v[44:45], v[74:75], v[162:163], v[88:89] op_sel:[0,0,1] op_sel_hi:[1,0,0]
	v_mfma_f32_16x16x32_f16 v[38:41], v[180:183], v[172:175], v[38:41]
	v_cvt_pk_f16_f32 v88, v42, v45
	v_mfma_f32_16x16x32_f16 v[42:45], v[180:183], v[148:151], v[62:65]
	s_nop 2
	v_mul_f32_e64 v62, v76, v120
	v_mul_f32_e64 v63, v77, v120
	v_mfma_f32_16x16x32_f16 v[66:69], v[184:187], v[172:175], v[66:69]
	v_fma_f32 v64, v76, v122, -v63
	v_fma_f32 v65, v77, v122, -v62
	v_pk_fma_f32 v[62:63], v[76:77], v[122:123], v[62:63] op_sel:[0,0,1] op_sel_hi:[1,0,0]
	s_nop 0
	v_cvt_pk_f16_f32 v89, v64, v63
	v_lshl_add_u64 v[62:63], s[12:13], 0, v[124:125]
	v_lshl_add_u64 v[62:63], v[62:63], 0, v[16:17]
	v_lshl_add_u64 v[106:107], v[62:63], 0, v[138:139]
	s_waitcnt vmcnt(6)
	v_pk_mul_f32 v[62:63], v[42:43], v[168:169] op_sel_hi:[1,0]
	global_store_dwordx4 v[106:107], v[86:89], off sc1
	s_waitcnt vmcnt(6)
	v_pk_fma_f32 v[64:65], v[42:43], v[164:165], v[62:63] op_sel:[0,0,1] op_sel_hi:[1,1,0] neg_lo:[0,0,1] neg_hi:[0,0,1]
	v_pk_fma_f32 v[42:43], v[42:43], v[164:165], v[62:63] op_sel:[0,0,1] op_sel_hi:[1,0,0]
	v_pk_mul_f32 v[62:63], v[44:45], v[168:169] op_sel:[0,1]
	v_cvt_pk_f16_f32 v42, v64, v43
	v_pk_fma_f32 v[74:75], v[44:45], v[164:165], v[62:63] op_sel:[0,1,1] op_sel_hi:[1,1,0] neg_lo:[0,0,1] neg_hi:[0,0,1]
	v_pk_fma_f32 v[44:45], v[44:45], v[164:165], v[62:63] op_sel:[0,1,1] op_sel_hi:[1,1,0]
	v_mov_b32_e32 v86, v171
	v_cvt_pk_f16_f32 v43, v74, v45
	v_pk_mul_f32 v[44:45], v[58:59], v[170:171] op_sel_hi:[1,0]
	v_mov_b32_e32 v88, v167
	v_pk_fma_f32 v[74:75], v[58:59], v[166:167], v[44:45] op_sel:[0,0,1] op_sel_hi:[1,1,0] neg_lo:[0,0,1] neg_hi:[0,0,1]
	v_pk_fma_f32 v[44:45], v[58:59], v[166:167], v[44:45] op_sel:[0,0,1] op_sel_hi:[1,0,0]
	v_pk_mul_f32 v[58:59], v[60:61], v[86:87] op_sel_hi:[1,0]
	v_cvt_pk_f16_f32 v44, v74, v45
	v_pk_fma_f32 v[108:109], v[60:61], v[88:89], v[58:59] op_sel:[0,0,1] op_sel_hi:[1,0,0] neg_lo:[0,0,1] neg_hi:[0,0,1]
	v_pk_fma_f32 v[58:59], v[60:61], v[88:89], v[58:59] op_sel:[0,0,1] op_sel_hi:[1,0,0]
	v_mfma_f32_16x16x32_f16 v[74:77], v[194:197], v[172:175], v[78:81]
	v_cvt_pk_f16_f32 v45, v108, v59
	global_store_dwordx4 v[126:127], v[42:45], off offset:2048 sc1
	v_pk_mul_f32 v[58:59], v[54:55], v[168:169] op_sel_hi:[1,0]
	v_mfma_f32_16x16x32_f16 v[22:25], v[180:183], v[176:179], v[22:25]
	v_fma_f32 v78, v54, v164, -v59
	v_fma_f32 v79, v55, v165, -v58
	v_pk_fma_f32 v[54:55], v[54:55], v[164:165], v[58:59] op_sel:[0,0,1] op_sel_hi:[1,0,0]
	v_mfma_f32_16x16x32_f16 v[42:45], v[198:201], v[172:175], v[82:85]
	v_cvt_pk_f16_f32 v54, v78, v55
	s_nop 1
	v_pk_mul_f32 v[82:83], v[56:57], v[168:169] op_sel:[0,1]
	v_mfma_f32_16x16x32_f16 v[30:33], v[194:197], v[176:179], v[30:33]
	v_fma_f32 v84, v56, v165, -v83
	v_fma_f32 v85, v57, v165, -v82
	v_pk_fma_f32 v[56:57], v[56:57], v[164:165], v[82:83] op_sel:[0,1,1] op_sel_hi:[1,1,0]
	s_nop 0
	v_cvt_pk_f16_f32 v55, v84, v57
	v_pk_mul_f32 v[56:57], v[50:51], v[170:171] op_sel_hi:[1,0]
	v_mfma_f32_16x16x32_f16 v[26:29], v[198:201], v[176:179], v[26:29]
	v_fma_f32 v82, v50, v166, -v57
	v_fma_f32 v83, v51, v167, -v56
	v_pk_fma_f32 v[50:51], v[50:51], v[166:167], v[56:57] op_sel:[0,0,1] op_sel_hi:[1,0,0]
	s_nop 0
	v_cvt_pk_f16_f32 v56, v82, v51
	v_pk_mul_f32 v[50:51], v[52:53], v[86:87] op_sel_hi:[1,0]
	v_mfma_f32_16x16x32_f16 v[82:85], v[184:187], v[176:179], v[102:105]
	v_fma_f32 v86, v52, v88, -v51
	v_fma_f32 v87, v53, v88, -v50
	v_pk_fma_f32 v[50:51], v[52:53], v[88:89], v[50:51] op_sel:[0,0,1] op_sel_hi:[1,0,0]
	s_nop 0
	v_cvt_pk_f16_f32 v57, v86, v51
	global_store_dwordx4 v[106:107], v[54:57], off offset:2048 sc1
	s_waitcnt vmcnt(7)
	v_pk_mul_f32 v[50:51], v[38:39], v[210:211] op_sel_hi:[1,0]
	v_mfma_f32_16x16x32_f16 v[70:73], v[140:143], v[202:205], v[70:73]
	v_mul_f32_e64 v56, v40, v211
	v_mul_f32_e64 v57, v41, v211
	s_waitcnt vmcnt(6)
	v_pk_fma_f32 v[52:53], v[38:39], v[4:5], v[50:51] op_sel:[0,0,1] op_sel_hi:[1,1,0] neg_lo:[0,0,1] neg_hi:[0,0,1]
	v_pk_fma_f32 v[38:39], v[38:39], v[4:5], v[50:51] op_sel:[0,0,1] op_sel_hi:[1,0,0]
	v_pk_fma_f32 v[86:87], v[40:41], v[4:5], v[56:57] op_sel:[0,1,1] op_sel_hi:[1,1,0] neg_lo:[0,0,1] neg_hi:[0,0,1]
	v_pk_fma_f32 v[40:41], v[40:41], v[4:5], v[56:57] op_sel:[0,1,1] op_sel_hi:[1,1,0]
	v_cvt_pk_f16_f32 v38, v52, v39
	v_cvt_pk_f16_f32 v39, v86, v41
	v_pk_mul_f32 v[40:41], v[66:67], v[212:213] op_sel_hi:[1,0]
	v_or_b32_e32 v54, 0x800, v118
	v_pk_fma_f32 v[56:57], v[66:67], v[6:7], v[40:41] op_sel:[0,0,1] op_sel_hi:[1,1,0] neg_lo:[0,0,1] neg_hi:[0,0,1]
	v_pk_fma_f32 v[40:41], v[66:67], v[6:7], v[40:41] op_sel:[0,0,1] op_sel_hi:[1,0,0]
	v_mov_b32_e32 v55, v119
	v_cvt_pk_f16_f32 v40, v56, v41
	v_mov_b32_e32 v56, v213
	v_pk_mul_f32 v[66:67], v[68:69], v[56:57] op_sel_hi:[1,0]
	v_mov_b32_e32 v86, v7
	v_pk_fma_f32 v[88:89], v[68:69], v[86:87], v[66:67] op_sel:[0,0,1] op_sel_hi:[1,0,0] neg_lo:[0,0,1] neg_hi:[0,0,1]
	v_pk_fma_f32 v[66:67], v[68:69], v[86:87], v[66:67] op_sel:[0,0,1] op_sel_hi:[1,0,0]
	v_lshlrev_b64 v[54:55], 1, v[54:55]
	v_cvt_pk_f16_f32 v41, v88, v67
	v_lshl_add_u64 v[66:67], s[10:11], 0, v[54:55]
	v_lshl_add_u64 v[66:67], v[66:67], 0, v[16:17]
	v_lshl_add_u64 v[66:67], v[66:67], 0, v[138:139]
	global_store_dwordx4 v[66:67], v[38:41], off sc1
	v_or_b32_e32 v118, 0xc00, v118
	v_mfma_f32_16x16x32_f16 v[46:49], v[148:151], v[202:205], v[46:49]
	v_mul_f32_e64 v38, v74, v210
	v_mul_f32_e64 v39, v75, v210
	v_pk_fma_f32 v[40:41], v[74:75], v[4:5], v[38:39] op_sel:[0,0,1] op_sel_hi:[1,1,0] neg_lo:[0,0,1] neg_hi:[0,0,1]
	v_pk_fma_f32 v[38:39], v[74:75], v[4:5], v[38:39] op_sel:[0,0,1] op_sel_hi:[1,0,0]
	v_mfma_f32_16x16x32_f16 v[58:61], v[172:175], v[202:205], v[90:93]
	v_cvt_pk_f16_f32 v38, v40, v39
	v_pk_mul_f32 v[40:41], v[76:77], v[210:211] op_sel:[0,1]
	s_nop 0
	v_pk_fma_f32 v[66:67], v[76:77], v[4:5], v[40:41] op_sel:[0,1,1] op_sel_hi:[1,1,0] neg_lo:[0,0,1] neg_hi:[0,0,1]
	v_pk_fma_f32 v[4:5], v[76:77], v[4:5], v[40:41] op_sel:[0,1,1] op_sel_hi:[1,1,0]
	v_mfma_f32_16x16x32_f16 v[34:37], v[176:179], v[202:205], v[34:37]
	v_cvt_pk_f16_f32 v39, v66, v5
	v_pk_mul_f32 v[4:5], v[42:43], v[212:213] op_sel_hi:[1,0]
	s_nop 0
	v_pk_fma_f32 v[40:41], v[42:43], v[6:7], v[4:5] op_sel:[0,0,1] op_sel_hi:[1,1,0] neg_lo:[0,0,1] neg_hi:[0,0,1]
	v_pk_fma_f32 v[4:5], v[42:43], v[6:7], v[4:5] op_sel:[0,0,1] op_sel_hi:[1,0,0]
	v_mfma_f32_16x16x32_f16 v[62:65], v[148:151], v[206:209], v[110:113]
	v_cvt_pk_f16_f32 v40, v40, v5
	v_pk_mul_f32 v[4:5], v[44:45], v[56:57] op_sel_hi:[1,0]
	s_nop 0
	v_pk_fma_f32 v[6:7], v[44:45], v[86:87], v[4:5] op_sel:[0,0,1] op_sel_hi:[1,0,0] neg_lo:[0,0,1] neg_hi:[0,0,1]
	v_pk_fma_f32 v[4:5], v[44:45], v[86:87], v[4:5] op_sel:[0,0,1] op_sel_hi:[1,0,0]
	v_mfma_f32_16x16x32_f16 v[78:81], v[172:175], v[206:209], v[94:97]
	v_cvt_pk_f16_f32 v41, v6, v5
	v_lshl_add_u64 v[4:5], s[12:13], 0, v[54:55]
	v_lshl_add_u64 v[4:5], v[4:5], 0, v[16:17]
	v_lshl_add_u64 v[4:5], v[4:5], 0, v[138:139]
	global_store_dwordx4 v[4:5], v[38:41], off sc1
	s_waitcnt vmcnt(7)
	v_pk_mul_f32 v[4:5], v[22:23], v[8:9] op_sel_hi:[1,0]
	v_mfma_f32_16x16x32_f16 v[50:53], v[176:179], v[206:209], v[98:101]
	s_waitcnt vmcnt(6)
	v_pk_fma_f32 v[6:7], v[22:23], v[0:1], v[4:5] op_sel:[0,0,1] op_sel_hi:[1,1,0] neg_lo:[0,0,1] neg_hi:[0,0,1]
	v_pk_fma_f32 v[4:5], v[22:23], v[0:1], v[4:5] op_sel:[0,0,1] op_sel_hi:[1,0,0]
	v_mov_b32_e32 v38, v3
	v_cvt_pk_f16_f32 v4, v6, v5
	v_pk_mul_f32 v[6:7], v[24:25], v[8:9] op_sel:[0,1]
	s_nop 0
	v_pk_fma_f32 v[22:23], v[24:25], v[0:1], v[6:7] op_sel:[0,1,1] op_sel_hi:[1,1,0] neg_lo:[0,0,1] neg_hi:[0,0,1]
	v_pk_fma_f32 v[6:7], v[24:25], v[0:1], v[6:7] op_sel:[0,1,1] op_sel_hi:[1,1,0]
	s_nop 0
	v_cvt_pk_f16_f32 v5, v22, v7
	v_pk_mul_f32 v[6:7], v[82:83], v[10:11] op_sel_hi:[1,0]
	s_nop 0
	v_pk_fma_f32 v[22:23], v[82:83], v[2:3], v[6:7] op_sel:[0,0,1] op_sel_hi:[1,1,0] neg_lo:[0,0,1] neg_hi:[0,0,1]
	v_pk_fma_f32 v[6:7], v[82:83], v[2:3], v[6:7] op_sel:[0,0,1] op_sel_hi:[1,0,0]
	s_nop 0
	v_cvt_pk_f16_f32 v6, v22, v7
	v_mov_b32_e32 v22, v11
	v_pk_mul_f32 v[24:25], v[84:85], v[22:23] op_sel_hi:[1,0]
	s_nop 0
	v_pk_fma_f32 v[40:41], v[84:85], v[38:39], v[24:25] op_sel:[0,0,1] op_sel_hi:[1,0,0] neg_lo:[0,0,1] neg_hi:[0,0,1]
	v_pk_fma_f32 v[24:25], v[84:85], v[38:39], v[24:25] op_sel:[0,0,1] op_sel_hi:[1,0,0]
	s_nop 0
	v_cvt_pk_f16_f32 v7, v40, v25
	v_lshlrev_b64 v[24:25], 1, v[118:119]
	v_lshl_add_u64 v[40:41], s[10:11], 0, v[24:25]
	v_lshl_add_u64 v[40:41], v[40:41], 0, v[16:17]
	v_lshl_add_u64 v[40:41], v[40:41], 0, v[138:139]
	global_store_dwordx4 v[40:41], v[4:7], off sc1
	s_nop 1
	v_pk_mul_f32 v[4:5], v[30:31], v[8:9] op_sel_hi:[1,0]
	s_nop 0
	v_pk_fma_f32 v[6:7], v[30:31], v[0:1], v[4:5] op_sel:[0,0,1] op_sel_hi:[1,1,0] neg_lo:[0,0,1] neg_hi:[0,0,1]
	v_pk_fma_f32 v[4:5], v[30:31], v[0:1], v[4:5] op_sel:[0,0,1] op_sel_hi:[1,0,0]
	s_nop 0
	v_cvt_pk_f16_f32 v4, v6, v5
	v_pk_mul_f32 v[6:7], v[32:33], v[8:9] op_sel:[0,1]
	s_nop 0
	v_pk_fma_f32 v[8:9], v[32:33], v[0:1], v[6:7] op_sel:[0,1,1] op_sel_hi:[1,1,0] neg_lo:[0,0,1] neg_hi:[0,0,1]
	v_pk_fma_f32 v[0:1], v[32:33], v[0:1], v[6:7] op_sel:[0,1,1] op_sel_hi:[1,1,0]
	s_nop 0
	v_cvt_pk_f16_f32 v5, v8, v1
	v_pk_mul_f32 v[0:1], v[26:27], v[10:11] op_sel_hi:[1,0]
	s_nop 0
	v_pk_fma_f32 v[6:7], v[26:27], v[2:3], v[0:1] op_sel:[0,0,1] op_sel_hi:[1,1,0] neg_lo:[0,0,1] neg_hi:[0,0,1]
	v_pk_fma_f32 v[0:1], v[26:27], v[2:3], v[0:1] op_sel:[0,0,1] op_sel_hi:[1,0,0]
	s_nop 0
	v_cvt_pk_f16_f32 v6, v6, v1
	v_pk_mul_f32 v[0:1], v[28:29], v[22:23] op_sel_hi:[1,0]
	s_nop 0
	v_pk_fma_f32 v[2:3], v[28:29], v[38:39], v[0:1] op_sel:[0,0,1] op_sel_hi:[1,0,0] neg_lo:[0,0,1] neg_hi:[0,0,1]
	v_pk_fma_f32 v[0:1], v[28:29], v[38:39], v[0:1] op_sel:[0,0,1] op_sel_hi:[1,0,0]
	v_cvt_pk_f16_f32 v3, v48, v49
	v_cvt_pk_f16_f32 v7, v2, v1
	v_lshl_add_u64 v[0:1], s[12:13], 0, v[24:25]
	v_lshl_add_u64 v[0:1], v[0:1], 0, v[16:17]
	v_lshl_add_u64 v[0:1], v[0:1], 0, v[138:139]
	global_store_dwordx4 v[0:1], v[4:7], off sc1
	v_lshlrev_b64 v[0:1], 18, v[18:19]
	v_lshlrev_b32_e32 v2, 7, v145
	v_lshl_add_u64 v[0:1], s[14:15], 0, v[0:1]
	v_and_b32_e32 v16, 0x3e000, v2
	v_lshl_add_u64 v[0:1], v[0:1], 0, v[16:17]
	v_lshlrev_b32_e32 v16, 4, v20
	v_lshl_add_u64 v[4:5], v[0:1], 0, v[16:17]
	v_lshlrev_b32_e32 v16, 12, v144
	v_cvt_pk_f16_f32 v2, v46, v47
	v_cvt_pk_f16_f32 v1, v72, v73
	v_cvt_pk_f16_f32 v0, v70, v71
	v_lshl_add_u64 v[4:5], v[4:5], 0, v[16:17]
	global_store_dwordx4 v[4:5], v[0:3], off sc1
	s_nop 1
	v_cvt_pk_f16_f32 v3, v36, v37
	v_cvt_pk_f16_f32 v2, v34, v35
	v_cvt_pk_f16_f32 v1, v60, v61
	v_cvt_pk_f16_f32 v0, v58, v59
	global_store_dwordx4 v[4:5], v[0:3], off offset:1024 sc1
	s_nop 1
	v_cvt_pk_f16_f32 v3, v64, v65
	v_cvt_pk_f16_f32 v2, v62, v63
	v_cvt_pk_f16_f32 v1, v14, v15
	v_cvt_pk_f16_f32 v0, v12, v13
	global_store_dwordx4 v[4:5], v[0:3], off offset:2048 sc1
	s_nop 1
	v_cvt_pk_f16_f32 v3, v52, v53
	v_cvt_pk_f16_f32 v2, v50, v51
	v_cvt_pk_f16_f32 v1, v80, v81
	v_cvt_pk_f16_f32 v0, v78, v79
	global_store_dwordx4 v[4:5], v[0:3], off offset:3072 sc1
	s_endpgm
	.p2align	8
